# speedup vs baseline: 1.0015x; 1.0015x over previous
_Z11center_mainPKfPKcS0_Pf:
	s_load_dwordx4 s[4:7], s[0:1], 0x0
	s_load_dwordx4 s[8:11], s[0:1], 0x10
	s_and_b32 s3, s2, 7
	s_lshr_b32 s12, s2, 3
	s_mov_b32 s30, s2
	v_lshrrev_b32_e32 v1, 6, v0
	v_and_b32_e32 v2, 63, v0
	v_bfe_u32 v3, v0, 3, 3
	v_and_b32_e32 v4, 7, v0
	v_lshrrev_b32_e32 v5, 7, v0
	v_bfe_u32 v6, v0, 6, 1
	v_lshl_or_b32 v7, v5, 3, v3
	v_lshlrev_b32_e32 v8, 10, v7
	v_lshl_or_b32 v8, v6, 9, v8
	v_lshl_or_b32 v226, v4, 4, v8
	v_lshlrev_b32_e32 v17, 15, v1
	v_lshl_or_b32 v227, v2, 5, v17
	v_lshlrev_b32_e32 v237, 3, v0
	s_lshl_b32 s13, s3, 22
	s_lshl_b32 s14, s12, 15
	s_add_u32 s13, s13, s14
	s_lshl_b32 s15, s3, 18
	s_lshl_b32 s28, s3, 12
	s_waitcnt lgkmcnt(0)
	s_add_u32 s16, s4, s13
	s_addc_u32 s17, s5, 0
	global_load_dwordx4 v[194:197], v226, s[16:17] offset:0 nt
	global_load_dwordx4 v[198:201], v226, s[16:17] offset:128 nt
	global_load_dwordx4 v[202:205], v226, s[16:17] offset:256 nt
	global_load_dwordx4 v[206:209], v226, s[16:17] offset:384 nt
	s_add_u32 s8, s8, s28
	s_addc_u32 s9, s9, 0
	global_load_dwordx2 v[238:239], v237, s[8:9]
	s_add_u32 s24, s6, s15
	s_addc_u32 s25, s7, 0
	s_add_u32 s32, s24, 0x1000
	s_addc_u32 s33, s25, 0
	s_add_u32 s34, s24, 0x2000
	s_addc_u32 s35, s25, 0
	s_add_u32 s36, s24, 0x3000
	s_addc_u32 s37, s25, 0
	s_add_u32 s38, s24, 0x4000
	s_addc_u32 s39, s25, 0
	s_add_u32 s40, s24, 0x5000
	s_addc_u32 s41, s25, 0
	s_add_u32 s42, s24, 0x6000
	s_addc_u32 s43, s25, 0
	s_add_u32 s44, s24, 0x7000
	s_addc_u32 s45, s25, 0
	global_load_dwordx4 v[34:37], v227, s[24:25] offset:0
	global_load_dwordx4 v[38:41], v227, s[24:25] offset:16
	global_load_dwordx4 v[26:29], v227, s[24:25] offset:2048
	global_load_dwordx4 v[30:33], v227, s[24:25] offset:2064
	global_load_dwordx4 v[50:53], v227, s[32:33] offset:0
	global_load_dwordx4 v[54:57], v227, s[32:33] offset:16
	global_load_dwordx4 v[42:45], v227, s[32:33] offset:2048
	global_load_dwordx4 v[46:49], v227, s[32:33] offset:2064
	global_load_dwordx4 v[18:21], v227, s[34:35] offset:0
	global_load_dwordx4 v[22:25], v227, s[34:35] offset:16
	global_load_dwordx4 v[130:133], v227, s[34:35] offset:2048
	global_load_dwordx4 v[134:137], v227, s[34:35] offset:2064
	global_load_dwordx4 v[122:125], v227, s[36:37] offset:0
	global_load_dwordx4 v[126:129], v227, s[36:37] offset:16
	global_load_dwordx4 v[138:141], v227, s[36:37] offset:2048
	global_load_dwordx4 v[142:145], v227, s[36:37] offset:2064
	global_load_dwordx4 v[98:101], v227, s[38:39] offset:0
	global_load_dwordx4 v[102:105], v227, s[38:39] offset:16
	global_load_dwordx4 v[90:93], v227, s[38:39] offset:2048
	global_load_dwordx4 v[94:97], v227, s[38:39] offset:2064
	global_load_dwordx4 v[114:117], v227, s[40:41] offset:0
	global_load_dwordx4 v[118:121], v227, s[40:41] offset:16
	global_load_dwordx4 v[106:109], v227, s[40:41] offset:2048
	global_load_dwordx4 v[110:113], v227, s[40:41] offset:2064
	global_load_dwordx4 v[58:61], v227, s[42:43] offset:0
	global_load_dwordx4 v[62:65], v227, s[42:43] offset:16
	global_load_dwordx4 v[66:69], v227, s[42:43] offset:2048
	global_load_dwordx4 v[70:73], v227, s[42:43] offset:2064
	global_load_dwordx4 v[74:77], v227, s[44:45] offset:0
	global_load_dwordx4 v[78:81], v227, s[44:45] offset:16
	global_load_dwordx4 v[82:85], v227, s[44:45] offset:2048
	global_load_dwordx4 v[86:89], v227, s[44:45] offset:2064
	s_add_u32 s18, s16, 0x100000
	s_addc_u32 s19, s17, 0
	s_add_u32 s20, s16, 0x200000
	s_addc_u32 s21, s17, 0
	s_add_u32 s22, s16, 0x300000
	s_addc_u32 s23, s17, 0
	v_mul_u32_u24_e32 v9, 0x110, v7
	v_lshl_add_u32 v9, v6, 7, v9
	v_lshl_add_u32 v228, v4, 4, v9
	v_lshlrev_b32_e32 v10, 6, v7
	v_lshl_or_b32 v10, v6, 5, v10
	v_lshl_or_b32 v229, v4, 2, v10
	v_and_b32_e32 v11, 31, v0
	v_bfe_u32 v12, v0, 5, 1
	v_mul_u32_u24_e32 v13, 0x110, v11
	v_lshl_add_u32 v230, v12, 5, v13
	v_lshlrev_b32_e32 v14, 9, v1
	v_lshl_or_b32 v231, v12, 4, v14
	v_xor_b32_e32 v15, 32, v2
	v_lshlrev_b32_e32 v232, 2, v15
	v_xor_b32_e32 v15, 16, v2
	v_lshlrev_b32_e32 v247, 2, v15
	v_lshlrev_b32_e32 v16, 7, v1
	v_lshl_or_b32 v233, v11, 2, v16
	v_mov_b32_e32 v234, 0x7f7f7f7f
	s_waitcnt vmcnt(32)
	ds_write_b64 v237, v[238:239] offset:34816
	v_mul_f32_e32 v244, v194, v194
	v_mul_f32_e32 v245, v198, v198
	v_cvt_pk_fp8_f32 v240, v194, v195
	v_cvt_pk_fp8_f32 v241, v198, v199
	v_cvt_pk_fp8_f32 v242, v202, v203
	v_cvt_pk_fp8_f32 v243, v206, v207
	v_fmac_f32_e32 v244, v195, v195
	v_fmac_f32_e32 v245, v199, v199
	v_fmac_f32_e32 v244, v196, v196
	v_fmac_f32_e32 v245, v200, v200
	v_fmac_f32_e32 v244, v197, v197
	v_fmac_f32_e32 v245, v201, v201
	v_fmac_f32_e32 v244, v202, v202
	v_fmac_f32_e32 v245, v206, v206
	v_fmac_f32_e32 v244, v203, v203
	v_fmac_f32_e32 v245, v207, v207
	v_fmac_f32_e32 v244, v204, v204
	v_fmac_f32_e32 v245, v208, v208
	v_fmac_f32_e32 v244, v205, v205
	v_fmac_f32_e32 v245, v209, v209
	v_cvt_pk_fp8_f32 v240, v196, v197 op_sel:[0,0,1]
	v_cvt_pk_fp8_f32 v241, v200, v201 op_sel:[0,0,1]
	v_cvt_pk_fp8_f32 v242, v204, v205 op_sel:[0,0,1]
	v_cvt_pk_fp8_f32 v243, v208, v209 op_sel:[0,0,1]
	v_add_f32_e32 v244, v244, v245
	s_nop 0
	ds_write_b128 v228, v[240:243] offset:0
	ds_write_b32 v229, v244 offset:38912
	global_load_dwordx4 v[210:213], v226, s[18:19] offset:0 nt
	global_load_dwordx4 v[214:217], v226, s[18:19] offset:128 nt
	global_load_dwordx4 v[218:221], v226, s[18:19] offset:256 nt
	global_load_dwordx4 v[222:225], v226, s[18:19] offset:384 nt
	s_waitcnt lgkmcnt(0)
	s_barrier
	ds_read_b128 v[162:165], v230 offset:0
	ds_read_b128 v[166:169], v230 offset:16
	ds_read_b128 v[2:5], v231 offset:34816
	ds_read_b128 v[6:9], v231 offset:34848
	ds_read_b128 v[10:13], v231 offset:34880
	ds_read_b128 v[14:17], v231 offset:34912
	ds_read_b128 v[170:173], v230 offset:64
	ds_read_b128 v[174:177], v230 offset:80
	ds_read_b128 v[178:181], v230 offset:128
	ds_read_b128 v[182:185], v230 offset:144
	ds_read_b128 v[186:189], v230 offset:192
	ds_read_b128 v[190:193], v230 offset:208
	s_waitcnt vmcnt(34) lgkmcnt(6)
	v_mfma_scale_f32_32x32x64_f8f6f4 v[2:17], v[34:41], v[162:169], v[2:17], v234, v234 op_sel_hi:[0,0,0]
	s_waitcnt vmcnt(32) lgkmcnt(4)
	v_mfma_scale_f32_32x32x64_f8f6f4 v[2:17], v[26:33], v[170:177], v[2:17], v234, v234 op_sel_hi:[0,0,0]
	s_waitcnt vmcnt(30) lgkmcnt(2)
	v_mfma_scale_f32_32x32x64_f8f6f4 v[2:17], v[50:57], v[178:185], v[2:17], v234, v234 op_sel_hi:[0,0,0]
	s_waitcnt vmcnt(28) lgkmcnt(0)
	v_mfma_scale_f32_32x32x64_f8f6f4 v[2:17], v[42:49], v[186:193], v[2:17], v234, v234 op_sel_hi:[0,0,0]
	ds_read_b128 v[146:149], v231 offset:34944
	ds_read_b128 v[150:153], v231 offset:34976
	ds_read_b128 v[154:157], v231 offset:35008
	ds_read_b128 v[158:161], v231 offset:35040
	s_waitcnt vmcnt(26) lgkmcnt(0)
	v_mfma_scale_f32_32x32x64_f8f6f4 v[146:161], v[18:25], v[162:169], v[146:161], v234, v234 op_sel_hi:[0,0,0]
	s_waitcnt vmcnt(24)
	v_mfma_scale_f32_32x32x64_f8f6f4 v[146:161], v[130:137], v[170:177], v[146:161], v234, v234 op_sel_hi:[0,0,0]
	s_waitcnt vmcnt(22)
	v_mfma_scale_f32_32x32x64_f8f6f4 v[146:161], v[122:129], v[178:185], v[146:161], v234, v234 op_sel_hi:[0,0,0]
	s_waitcnt vmcnt(20)
	v_mfma_scale_f32_32x32x64_f8f6f4 v[146:161], v[138:145], v[186:193], v[146:161], v234, v234 op_sel_hi:[0,0,0]
	s_nop 15
	v_min3_f32 v2, v2, v3, v4
	v_min3_f32 v5, v5, v6, v7
	v_min3_f32 v8, v8, v9, v10
	v_min3_f32 v11, v11, v12, v13
	v_min3_f32 v14, v14, v15, v16
	v_min3_f32 v2, v2, v5, v8
	v_min3_f32 v11, v11, v14, v17
	v_min_f32_e32 v235, v2, v11
	ds_read_b128 v[2:5], v231 offset:35072
	ds_read_b128 v[6:9], v231 offset:35104
	ds_read_b128 v[10:13], v231 offset:35136
	ds_read_b128 v[14:17], v231 offset:35168
	s_waitcnt vmcnt(18) lgkmcnt(0)
	v_mfma_scale_f32_32x32x64_f8f6f4 v[2:17], v[98:105], v[162:169], v[2:17], v234, v234 op_sel_hi:[0,0,0]
	s_waitcnt vmcnt(16)
	v_mfma_scale_f32_32x32x64_f8f6f4 v[2:17], v[90:97], v[170:177], v[2:17], v234, v234 op_sel_hi:[0,0,0]
	s_waitcnt vmcnt(14)
	v_mfma_scale_f32_32x32x64_f8f6f4 v[2:17], v[114:121], v[178:185], v[2:17], v234, v234 op_sel_hi:[0,0,0]
	s_waitcnt vmcnt(12)
	v_mfma_scale_f32_32x32x64_f8f6f4 v[2:17], v[106:113], v[186:193], v[2:17], v234, v234 op_sel_hi:[0,0,0]
	s_nop 15
	v_min3_f32 v146, v146, v147, v148
	v_min3_f32 v149, v149, v150, v151
	v_min3_f32 v152, v152, v153, v154
	v_min3_f32 v155, v155, v156, v157
	v_min3_f32 v158, v158, v159, v160
	v_min3_f32 v146, v146, v149, v152
	v_min3_f32 v155, v155, v158, v161
	v_min3_f32 v235, v235, v146, v155
	ds_read_b128 v[146:149], v231 offset:35200
	ds_read_b128 v[150:153], v231 offset:35232
	ds_read_b128 v[154:157], v231 offset:35264
	ds_read_b128 v[158:161], v231 offset:35296
	s_waitcnt vmcnt(10) lgkmcnt(0)
	v_mfma_scale_f32_32x32x64_f8f6f4 v[146:161], v[58:65], v[162:169], v[146:161], v234, v234 op_sel_hi:[0,0,0]
	s_waitcnt vmcnt(8)
	v_mfma_scale_f32_32x32x64_f8f6f4 v[146:161], v[66:73], v[170:177], v[146:161], v234, v234 op_sel_hi:[0,0,0]
	s_waitcnt vmcnt(6)
	v_mfma_scale_f32_32x32x64_f8f6f4 v[146:161], v[74:81], v[178:185], v[146:161], v234, v234 op_sel_hi:[0,0,0]
	s_waitcnt vmcnt(4)
	v_mfma_scale_f32_32x32x64_f8f6f4 v[146:161], v[82:89], v[186:193], v[146:161], v234, v234 op_sel_hi:[0,0,0]
	global_load_dwordx4 v[194:197], v226, s[20:21] offset:0 nt
	global_load_dwordx4 v[198:201], v226, s[20:21] offset:128 nt
	global_load_dwordx4 v[202:205], v226, s[20:21] offset:256 nt
	global_load_dwordx4 v[206:209], v226, s[20:21] offset:384 nt
	s_waitcnt vmcnt(4)
	v_mul_f32_e32 v244, v210, v210
	v_mul_f32_e32 v245, v214, v214
	v_cvt_pk_fp8_f32 v240, v210, v211
	v_cvt_pk_fp8_f32 v241, v214, v215
	v_cvt_pk_fp8_f32 v242, v218, v219
	v_cvt_pk_fp8_f32 v243, v222, v223
	v_fmac_f32_e32 v244, v211, v211
	v_fmac_f32_e32 v245, v215, v215
	v_fmac_f32_e32 v244, v212, v212
	v_fmac_f32_e32 v245, v216, v216
	v_fmac_f32_e32 v244, v213, v213
	v_fmac_f32_e32 v245, v217, v217
	v_fmac_f32_e32 v244, v218, v218
	v_fmac_f32_e32 v245, v222, v222
	v_fmac_f32_e32 v244, v219, v219
	v_fmac_f32_e32 v245, v223, v223
	v_fmac_f32_e32 v244, v220, v220
	v_fmac_f32_e32 v245, v224, v224
	v_fmac_f32_e32 v244, v221, v221
	v_fmac_f32_e32 v245, v225, v225
	v_cvt_pk_fp8_f32 v240, v212, v213 op_sel:[0,0,1]
	v_cvt_pk_fp8_f32 v241, v216, v217 op_sel:[0,0,1]
	v_cvt_pk_fp8_f32 v242, v220, v221 op_sel:[0,0,1]
	v_cvt_pk_fp8_f32 v243, v224, v225 op_sel:[0,0,1]
	v_add_f32_e32 v244, v244, v245
	s_nop 0
	ds_write_b128 v228, v[240:243] offset:8704
	ds_write_b32 v229, v244 offset:40960
	v_min3_f32 v2, v2, v3, v4
	v_min3_f32 v5, v5, v6, v7
	v_min3_f32 v8, v8, v9, v10
	v_min3_f32 v11, v11, v12, v13
	v_min3_f32 v14, v14, v15, v16
	v_min3_f32 v2, v2, v5, v8
	v_min3_f32 v11, v11, v14, v17
	v_min3_f32 v235, v235, v2, v11
	ds_read_b128 v[2:5], v231 offset:34816
	ds_read_b128 v[6:9], v231 offset:34848
	ds_read_b128 v[10:13], v231 offset:34880
	ds_read_b128 v[14:17], v231 offset:34912
	s_waitcnt lgkmcnt(0)
	s_barrier
	ds_read_b128 v[162:165], v230 offset:8704
	ds_read_b128 v[166:169], v230 offset:8720
	ds_read_b128 v[170:173], v230 offset:8768
	ds_read_b128 v[174:177], v230 offset:8784
	ds_read_b128 v[178:181], v230 offset:8832
	ds_read_b128 v[182:185], v230 offset:8848
	ds_read_b128 v[186:189], v230 offset:8896
	ds_read_b128 v[190:193], v230 offset:8912
	s_waitcnt lgkmcnt(6)
	v_mfma_scale_f32_32x32x64_f8f6f4 v[2:17], v[34:41], v[162:169], v[2:17], v234, v234 op_sel_hi:[0,0,0]
	s_waitcnt lgkmcnt(4)
	v_mfma_scale_f32_32x32x64_f8f6f4 v[2:17], v[26:33], v[170:177], v[2:17], v234, v234 op_sel_hi:[0,0,0]
	s_waitcnt lgkmcnt(2)
	v_mfma_scale_f32_32x32x64_f8f6f4 v[2:17], v[50:57], v[178:185], v[2:17], v234, v234 op_sel_hi:[0,0,0]
	s_waitcnt lgkmcnt(0)
	v_mfma_scale_f32_32x32x64_f8f6f4 v[2:17], v[42:49], v[186:193], v[2:17], v234, v234 op_sel_hi:[0,0,0]
	s_nop 15
	v_min3_f32 v146, v146, v147, v148
	v_min3_f32 v149, v149, v150, v151
	v_min3_f32 v152, v152, v153, v154
	v_min3_f32 v155, v155, v156, v157
	v_min3_f32 v158, v158, v159, v160
	v_min3_f32 v146, v146, v149, v152
	v_min3_f32 v155, v155, v158, v161
	v_min3_f32 v235, v235, v146, v155
	ds_bpermute_b32 v246, v232, v235
	s_waitcnt lgkmcnt(0)
	v_min_f32_e32 v246, v235, v246
	ds_write_b32 v233, v246 offset:47104
	ds_read_b128 v[146:149], v231 offset:34944
	ds_read_b128 v[150:153], v231 offset:34976
	ds_read_b128 v[154:157], v231 offset:35008
	ds_read_b128 v[158:161], v231 offset:35040
	s_waitcnt lgkmcnt(0)
	v_mfma_scale_f32_32x32x64_f8f6f4 v[146:161], v[18:25], v[162:169], v[146:161], v234, v234 op_sel_hi:[0,0,0]
	v_mfma_scale_f32_32x32x64_f8f6f4 v[146:161], v[130:137], v[170:177], v[146:161], v234, v234 op_sel_hi:[0,0,0]
	v_mfma_scale_f32_32x32x64_f8f6f4 v[146:161], v[122:129], v[178:185], v[146:161], v234, v234 op_sel_hi:[0,0,0]
	v_mfma_scale_f32_32x32x64_f8f6f4 v[146:161], v[138:145], v[186:193], v[146:161], v234, v234 op_sel_hi:[0,0,0]
	s_nop 15
	v_min3_f32 v2, v2, v3, v4
	v_min3_f32 v5, v5, v6, v7
	v_min3_f32 v8, v8, v9, v10
	v_min3_f32 v11, v11, v12, v13
	v_min3_f32 v14, v14, v15, v16
	v_min3_f32 v2, v2, v5, v8
	v_min3_f32 v11, v11, v14, v17
	v_min_f32_e32 v236, v2, v11
	ds_read_b128 v[2:5], v231 offset:35072
	ds_read_b128 v[6:9], v231 offset:35104
	ds_read_b128 v[10:13], v231 offset:35136
	ds_read_b128 v[14:17], v231 offset:35168
	s_waitcnt lgkmcnt(0)
	v_mfma_scale_f32_32x32x64_f8f6f4 v[2:17], v[98:105], v[162:169], v[2:17], v234, v234 op_sel_hi:[0,0,0]
	v_mfma_scale_f32_32x32x64_f8f6f4 v[2:17], v[90:97], v[170:177], v[2:17], v234, v234 op_sel_hi:[0,0,0]
	v_mfma_scale_f32_32x32x64_f8f6f4 v[2:17], v[114:121], v[178:185], v[2:17], v234, v234 op_sel_hi:[0,0,0]
	v_mfma_scale_f32_32x32x64_f8f6f4 v[2:17], v[106:113], v[186:193], v[2:17], v234, v234 op_sel_hi:[0,0,0]
	s_nop 15
	v_min3_f32 v146, v146, v147, v148
	v_min3_f32 v149, v149, v150, v151
	v_min3_f32 v152, v152, v153, v154
	v_min3_f32 v155, v155, v156, v157
	v_min3_f32 v158, v158, v159, v160
	v_min3_f32 v146, v146, v149, v152
	v_min3_f32 v155, v155, v158, v161
	v_min3_f32 v236, v236, v146, v155
	ds_read_b128 v[146:149], v231 offset:35200
	ds_read_b128 v[150:153], v231 offset:35232
	ds_read_b128 v[154:157], v231 offset:35264
	ds_read_b128 v[158:161], v231 offset:35296
	s_waitcnt lgkmcnt(0)
	v_mfma_scale_f32_32x32x64_f8f6f4 v[146:161], v[58:65], v[162:169], v[146:161], v234, v234 op_sel_hi:[0,0,0]
	v_mfma_scale_f32_32x32x64_f8f6f4 v[146:161], v[66:73], v[170:177], v[146:161], v234, v234 op_sel_hi:[0,0,0]
	v_mfma_scale_f32_32x32x64_f8f6f4 v[146:161], v[74:81], v[178:185], v[146:161], v234, v234 op_sel_hi:[0,0,0]
	v_mfma_scale_f32_32x32x64_f8f6f4 v[146:161], v[82:89], v[186:193], v[146:161], v234, v234 op_sel_hi:[0,0,0]
	global_load_dwordx4 v[210:213], v226, s[22:23] offset:0 nt
	global_load_dwordx4 v[214:217], v226, s[22:23] offset:128 nt
	global_load_dwordx4 v[218:221], v226, s[22:23] offset:256 nt
	global_load_dwordx4 v[222:225], v226, s[22:23] offset:384 nt
	s_waitcnt vmcnt(4)
	v_mul_f32_e32 v244, v194, v194
	v_mul_f32_e32 v245, v198, v198
	v_cvt_pk_fp8_f32 v240, v194, v195
	v_cvt_pk_fp8_f32 v241, v198, v199
	v_cvt_pk_fp8_f32 v242, v202, v203
	v_cvt_pk_fp8_f32 v243, v206, v207
	v_fmac_f32_e32 v244, v195, v195
	v_fmac_f32_e32 v245, v199, v199
	v_fmac_f32_e32 v244, v196, v196
	v_fmac_f32_e32 v245, v200, v200
	v_fmac_f32_e32 v244, v197, v197
	v_fmac_f32_e32 v245, v201, v201
	v_fmac_f32_e32 v244, v202, v202
	v_fmac_f32_e32 v245, v206, v206
	v_fmac_f32_e32 v244, v203, v203
	v_fmac_f32_e32 v245, v207, v207
	v_fmac_f32_e32 v244, v204, v204
	v_fmac_f32_e32 v245, v208, v208
	v_fmac_f32_e32 v244, v205, v205
	v_fmac_f32_e32 v245, v209, v209
	v_cvt_pk_fp8_f32 v240, v196, v197 op_sel:[0,0,1]
	v_cvt_pk_fp8_f32 v241, v200, v201 op_sel:[0,0,1]
	v_cvt_pk_fp8_f32 v242, v204, v205 op_sel:[0,0,1]
	v_cvt_pk_fp8_f32 v243, v208, v209 op_sel:[0,0,1]
	v_add_f32_e32 v244, v244, v245
	s_nop 0
	ds_write_b128 v228, v[240:243] offset:17408
	ds_write_b32 v229, v244 offset:43008
	v_min3_f32 v2, v2, v3, v4
	v_min3_f32 v5, v5, v6, v7
	v_min3_f32 v8, v8, v9, v10
	v_min3_f32 v11, v11, v12, v13
	v_min3_f32 v14, v14, v15, v16
	v_min3_f32 v2, v2, v5, v8
	v_min3_f32 v11, v11, v14, v17
	v_min3_f32 v236, v236, v2, v11
	ds_read_b128 v[2:5], v231 offset:34816
	ds_read_b128 v[6:9], v231 offset:34848
	ds_read_b128 v[10:13], v231 offset:34880
	ds_read_b128 v[14:17], v231 offset:34912
	s_waitcnt lgkmcnt(0)
	s_barrier
	ds_read_b128 v[162:165], v230 offset:17408
	ds_read_b128 v[166:169], v230 offset:17424
	ds_read_b128 v[170:173], v230 offset:17472
	ds_read_b128 v[174:177], v230 offset:17488
	ds_read_b128 v[178:181], v230 offset:17536
	ds_read_b128 v[182:185], v230 offset:17552
	ds_read_b128 v[186:189], v230 offset:17600
	ds_read_b128 v[190:193], v230 offset:17616
	s_waitcnt lgkmcnt(6)
	v_mfma_scale_f32_32x32x64_f8f6f4 v[2:17], v[34:41], v[162:169], v[2:17], v234, v234 op_sel_hi:[0,0,0]
	s_waitcnt lgkmcnt(4)
	v_mfma_scale_f32_32x32x64_f8f6f4 v[2:17], v[26:33], v[170:177], v[2:17], v234, v234 op_sel_hi:[0,0,0]
	s_waitcnt lgkmcnt(2)
	v_mfma_scale_f32_32x32x64_f8f6f4 v[2:17], v[50:57], v[178:185], v[2:17], v234, v234 op_sel_hi:[0,0,0]
	s_waitcnt lgkmcnt(0)
	v_mfma_scale_f32_32x32x64_f8f6f4 v[2:17], v[42:49], v[186:193], v[2:17], v234, v234 op_sel_hi:[0,0,0]
	s_nop 15
	v_min3_f32 v146, v146, v147, v148
	v_min3_f32 v149, v149, v150, v151
	v_min3_f32 v152, v152, v153, v154
	v_min3_f32 v155, v155, v156, v157
	v_min3_f32 v158, v158, v159, v160
	v_min3_f32 v146, v146, v149, v152
	v_min3_f32 v155, v155, v158, v161
	v_min3_f32 v236, v236, v146, v155
	ds_bpermute_b32 v246, v232, v236
	s_waitcnt lgkmcnt(0)
	v_min_f32_e32 v246, v236, v246
	ds_write_b32 v233, v246 offset:48128
	ds_read_b128 v[146:149], v231 offset:34944
	ds_read_b128 v[150:153], v231 offset:34976
	ds_read_b128 v[154:157], v231 offset:35008
	ds_read_b128 v[158:161], v231 offset:35040
	s_waitcnt lgkmcnt(0)
	v_mfma_scale_f32_32x32x64_f8f6f4 v[146:161], v[18:25], v[162:169], v[146:161], v234, v234 op_sel_hi:[0,0,0]
	v_mfma_scale_f32_32x32x64_f8f6f4 v[146:161], v[130:137], v[170:177], v[146:161], v234, v234 op_sel_hi:[0,0,0]
	v_mfma_scale_f32_32x32x64_f8f6f4 v[146:161], v[122:129], v[178:185], v[146:161], v234, v234 op_sel_hi:[0,0,0]
	v_mfma_scale_f32_32x32x64_f8f6f4 v[146:161], v[138:145], v[186:193], v[146:161], v234, v234 op_sel_hi:[0,0,0]
	s_nop 15
	v_min3_f32 v2, v2, v3, v4
	v_min3_f32 v5, v5, v6, v7
	v_min3_f32 v8, v8, v9, v10
	v_min3_f32 v11, v11, v12, v13
	v_min3_f32 v14, v14, v15, v16
	v_min3_f32 v2, v2, v5, v8
	v_min3_f32 v11, v11, v14, v17
	v_min_f32_e32 v235, v2, v11
	ds_read_b128 v[2:5], v231 offset:35072
	ds_read_b128 v[6:9], v231 offset:35104
	ds_read_b128 v[10:13], v231 offset:35136
	ds_read_b128 v[14:17], v231 offset:35168
	s_waitcnt lgkmcnt(0)
	v_mfma_scale_f32_32x32x64_f8f6f4 v[2:17], v[98:105], v[162:169], v[2:17], v234, v234 op_sel_hi:[0,0,0]
	v_mfma_scale_f32_32x32x64_f8f6f4 v[2:17], v[90:97], v[170:177], v[2:17], v234, v234 op_sel_hi:[0,0,0]
	v_mfma_scale_f32_32x32x64_f8f6f4 v[2:17], v[114:121], v[178:185], v[2:17], v234, v234 op_sel_hi:[0,0,0]
	v_mfma_scale_f32_32x32x64_f8f6f4 v[2:17], v[106:113], v[186:193], v[2:17], v234, v234 op_sel_hi:[0,0,0]
	s_nop 15
	v_min3_f32 v146, v146, v147, v148
	v_min3_f32 v149, v149, v150, v151
	v_min3_f32 v152, v152, v153, v154
	v_min3_f32 v155, v155, v156, v157
	v_min3_f32 v158, v158, v159, v160
	v_min3_f32 v146, v146, v149, v152
	v_min3_f32 v155, v155, v158, v161
	v_min3_f32 v235, v235, v146, v155
	ds_read_b128 v[146:149], v231 offset:35200
	ds_read_b128 v[150:153], v231 offset:35232
	ds_read_b128 v[154:157], v231 offset:35264
	ds_read_b128 v[158:161], v231 offset:35296
	s_waitcnt lgkmcnt(0)
	v_mfma_scale_f32_32x32x64_f8f6f4 v[146:161], v[58:65], v[162:169], v[146:161], v234, v234 op_sel_hi:[0,0,0]
	v_mfma_scale_f32_32x32x64_f8f6f4 v[146:161], v[66:73], v[170:177], v[146:161], v234, v234 op_sel_hi:[0,0,0]
	v_mfma_scale_f32_32x32x64_f8f6f4 v[146:161], v[74:81], v[178:185], v[146:161], v234, v234 op_sel_hi:[0,0,0]
	v_mfma_scale_f32_32x32x64_f8f6f4 v[146:161], v[82:89], v[186:193], v[146:161], v234, v234 op_sel_hi:[0,0,0]
	s_waitcnt vmcnt(0)
	v_mul_f32_e32 v244, v210, v210
	v_mul_f32_e32 v245, v214, v214
	v_cvt_pk_fp8_f32 v240, v210, v211
	v_cvt_pk_fp8_f32 v241, v214, v215
	v_cvt_pk_fp8_f32 v242, v218, v219
	v_cvt_pk_fp8_f32 v243, v222, v223
	v_fmac_f32_e32 v244, v211, v211
	v_fmac_f32_e32 v245, v215, v215
	v_fmac_f32_e32 v244, v212, v212
	v_fmac_f32_e32 v245, v216, v216
	v_fmac_f32_e32 v244, v213, v213
	v_fmac_f32_e32 v245, v217, v217
	v_fmac_f32_e32 v244, v218, v218
	v_fmac_f32_e32 v245, v222, v222
	v_fmac_f32_e32 v244, v219, v219
	v_fmac_f32_e32 v245, v223, v223
	v_fmac_f32_e32 v244, v220, v220
	v_fmac_f32_e32 v245, v224, v224
	v_fmac_f32_e32 v244, v221, v221
	v_fmac_f32_e32 v245, v225, v225
	v_cvt_pk_fp8_f32 v240, v212, v213 op_sel:[0,0,1]
	v_cvt_pk_fp8_f32 v241, v216, v217 op_sel:[0,0,1]
	v_cvt_pk_fp8_f32 v242, v220, v221 op_sel:[0,0,1]
	v_cvt_pk_fp8_f32 v243, v224, v225 op_sel:[0,0,1]
	v_add_f32_e32 v244, v244, v245
	s_nop 0
	ds_write_b128 v228, v[240:243] offset:26112
	ds_write_b32 v229, v244 offset:45056
	v_min3_f32 v2, v2, v3, v4
	v_min3_f32 v5, v5, v6, v7
	v_min3_f32 v8, v8, v9, v10
	v_min3_f32 v11, v11, v12, v13
	v_min3_f32 v14, v14, v15, v16
	v_min3_f32 v2, v2, v5, v8
	v_min3_f32 v11, v11, v14, v17
	v_min3_f32 v235, v235, v2, v11
	ds_read_b128 v[2:5], v231 offset:34816
	ds_read_b128 v[6:9], v231 offset:34848
	ds_read_b128 v[10:13], v231 offset:34880
	ds_read_b128 v[14:17], v231 offset:34912
	s_waitcnt lgkmcnt(0)
	s_barrier
	ds_read_b128 v[162:165], v230 offset:26112
	ds_read_b128 v[166:169], v230 offset:26128
	ds_read_b128 v[170:173], v230 offset:26176
	ds_read_b128 v[174:177], v230 offset:26192
	ds_read_b128 v[178:181], v230 offset:26240
	ds_read_b128 v[182:185], v230 offset:26256
	ds_read_b128 v[186:189], v230 offset:26304
	ds_read_b128 v[190:193], v230 offset:26320
	s_waitcnt lgkmcnt(6)
	v_mfma_scale_f32_32x32x64_f8f6f4 v[2:17], v[34:41], v[162:169], v[2:17], v234, v234 op_sel_hi:[0,0,0]
	s_waitcnt lgkmcnt(4)
	v_mfma_scale_f32_32x32x64_f8f6f4 v[2:17], v[26:33], v[170:177], v[2:17], v234, v234 op_sel_hi:[0,0,0]
	s_waitcnt lgkmcnt(2)
	v_mfma_scale_f32_32x32x64_f8f6f4 v[2:17], v[50:57], v[178:185], v[2:17], v234, v234 op_sel_hi:[0,0,0]
	s_waitcnt lgkmcnt(0)
	v_mfma_scale_f32_32x32x64_f8f6f4 v[2:17], v[42:49], v[186:193], v[2:17], v234, v234 op_sel_hi:[0,0,0]
	s_nop 15
	v_min3_f32 v146, v146, v147, v148
	v_min3_f32 v149, v149, v150, v151
	v_min3_f32 v152, v152, v153, v154
	v_min3_f32 v155, v155, v156, v157
	v_min3_f32 v158, v158, v159, v160
	v_min3_f32 v146, v146, v149, v152
	v_min3_f32 v155, v155, v158, v161
	v_min3_f32 v235, v235, v146, v155
	ds_bpermute_b32 v246, v232, v235
	s_waitcnt lgkmcnt(0)
	v_min_f32_e32 v246, v235, v246
	ds_write_b32 v233, v246 offset:49152
	ds_read_b128 v[146:149], v231 offset:34944
	ds_read_b128 v[150:153], v231 offset:34976
	ds_read_b128 v[154:157], v231 offset:35008
	ds_read_b128 v[158:161], v231 offset:35040
	s_waitcnt lgkmcnt(0)
	v_mfma_scale_f32_32x32x64_f8f6f4 v[146:161], v[18:25], v[162:169], v[146:161], v234, v234 op_sel_hi:[0,0,0]
	v_mfma_scale_f32_32x32x64_f8f6f4 v[146:161], v[130:137], v[170:177], v[146:161], v234, v234 op_sel_hi:[0,0,0]
	v_mfma_scale_f32_32x32x64_f8f6f4 v[146:161], v[122:129], v[178:185], v[146:161], v234, v234 op_sel_hi:[0,0,0]
	v_mfma_scale_f32_32x32x64_f8f6f4 v[146:161], v[138:145], v[186:193], v[146:161], v234, v234 op_sel_hi:[0,0,0]
	s_nop 15
	v_min3_f32 v2, v2, v3, v4
	v_min3_f32 v5, v5, v6, v7
	v_min3_f32 v8, v8, v9, v10
	v_min3_f32 v11, v11, v12, v13
	v_min3_f32 v14, v14, v15, v16
	v_min3_f32 v2, v2, v5, v8
	v_min3_f32 v11, v11, v14, v17
	v_min_f32_e32 v236, v2, v11
	ds_read_b128 v[2:5], v231 offset:35072
	ds_read_b128 v[6:9], v231 offset:35104
	ds_read_b128 v[10:13], v231 offset:35136
	ds_read_b128 v[14:17], v231 offset:35168
	s_waitcnt lgkmcnt(0)
	v_mfma_scale_f32_32x32x64_f8f6f4 v[2:17], v[98:105], v[162:169], v[2:17], v234, v234 op_sel_hi:[0,0,0]
	v_mfma_scale_f32_32x32x64_f8f6f4 v[2:17], v[90:97], v[170:177], v[2:17], v234, v234 op_sel_hi:[0,0,0]
	v_mfma_scale_f32_32x32x64_f8f6f4 v[2:17], v[114:121], v[178:185], v[2:17], v234, v234 op_sel_hi:[0,0,0]
	v_mfma_scale_f32_32x32x64_f8f6f4 v[2:17], v[106:113], v[186:193], v[2:17], v234, v234 op_sel_hi:[0,0,0]
	s_nop 15
	v_min3_f32 v146, v146, v147, v148
	v_min3_f32 v149, v149, v150, v151
	v_min3_f32 v152, v152, v153, v154
	v_min3_f32 v155, v155, v156, v157
	v_min3_f32 v158, v158, v159, v160
	v_min3_f32 v146, v146, v149, v152
	v_min3_f32 v155, v155, v158, v161
	v_min3_f32 v236, v236, v146, v155
	ds_read_b128 v[146:149], v231 offset:35200
	ds_read_b128 v[150:153], v231 offset:35232
	ds_read_b128 v[154:157], v231 offset:35264
	ds_read_b128 v[158:161], v231 offset:35296
	s_waitcnt lgkmcnt(0)
	v_mfma_scale_f32_32x32x64_f8f6f4 v[146:161], v[58:65], v[162:169], v[146:161], v234, v234 op_sel_hi:[0,0,0]
	v_mfma_scale_f32_32x32x64_f8f6f4 v[146:161], v[66:73], v[170:177], v[146:161], v234, v234 op_sel_hi:[0,0,0]
	v_mfma_scale_f32_32x32x64_f8f6f4 v[146:161], v[74:81], v[178:185], v[146:161], v234, v234 op_sel_hi:[0,0,0]
	v_mfma_scale_f32_32x32x64_f8f6f4 v[146:161], v[82:89], v[186:193], v[146:161], v234, v234 op_sel_hi:[0,0,0]
	v_cmp_gt_u32_e32 vcc, 0x80, v0
	s_and_saveexec_b64 s[34:35], vcc
	v_lshlrev_b32_e32 v36, 6, v0
	ds_read_b128 v[20:23], v36 offset:38912
	ds_read_b128 v[24:27], v36 offset:38928
	ds_read_b128 v[28:31], v36 offset:38944
	ds_read_b128 v[32:35], v36 offset:38960
	s_mov_b64 exec, s[34:35]
	s_nop 15
	v_min3_f32 v2, v2, v3, v4
	v_min3_f32 v5, v5, v6, v7
	v_min3_f32 v8, v8, v9, v10
	v_min3_f32 v11, v11, v12, v13
	v_min3_f32 v14, v14, v15, v16
	v_min3_f32 v2, v2, v5, v8
	v_min3_f32 v11, v11, v14, v17
	v_min3_f32 v236, v236, v2, v11
	s_nop 15
	s_nop 3
	v_min3_f32 v146, v146, v147, v148
	v_min3_f32 v149, v149, v150, v151
	v_min3_f32 v152, v152, v153, v154
	v_min3_f32 v155, v155, v156, v157
	v_min3_f32 v158, v158, v159, v160
	v_min3_f32 v146, v146, v149, v152
	v_min3_f32 v155, v155, v158, v161
	v_min3_f32 v236, v236, v146, v155
	ds_bpermute_b32 v246, v232, v236
	s_waitcnt lgkmcnt(0)
	v_min_f32_e32 v246, v236, v246
	ds_write_b32 v233, v246 offset:50176
	s_waitcnt lgkmcnt(0)
	s_barrier
	v_readfirstlane_b32 s2, v1
	s_nop 3
	s_cmp_gt_u32 s2, 1
	s_cbranch_scc1 .Lmain_end
	v_and_b32_e32 v2, 31, v0
	v_lshlrev_b32_e32 v3, 5, v0
	v_and_b32_e32 v3, 0xc00, v3
	v_lshl_or_b32 v8, v2, 2, v3
	v_add_u32_e32 v8, 0xb800, v8
	ds_read2_b32 v[2:3], v8 offset1:32
	ds_read2_b32 v[4:5], v8 offset0:64 offset1:96
	ds_read2_b32 v[6:7], v8 offset0:128 offset1:160
	ds_read2_b32 v[10:11], v8 offset0:192 offset1:224
	s_mov_b32 s8, 0xf800000
	s_lshr_b32 s2, s30, 3
	s_lshl_b32 s2, s2, 7
	s_add_u32 s2, s2, 0x300000
	s_add_u32 s6, s6, s2
	s_addc_u32 s7, s7, 0
	s_mov_b32 s4, 0
	s_mov_b32 s5, 0x41d00000
	s_mov_b32 s16, 0
	s_mov_b32 s17, 0x420e0000
	s_waitcnt lgkmcnt(0)
	v_min3_f32 v2, v2, v3, v4
	v_min3_f32 v5, v5, v6, v7
	v_min3_f32 v2, v2, v10, v11
	v_min_f32_e32 v2, v2, v5
	s_waitcnt lgkmcnt(0)
	v_add_f32_e32 v20, v20, v21
	v_add_f32_e32 v22, v22, v23
	v_add_f32_e32 v24, v24, v25
	v_add_f32_e32 v26, v26, v27
	v_add_f32_e32 v28, v28, v29
	v_add_f32_e32 v30, v30, v31
	v_add_f32_e32 v32, v32, v33
	v_add_f32_e32 v34, v34, v35
	v_add_f32_e32 v20, v20, v22
	v_add_f32_e32 v24, v24, v26
	v_add_f32_e32 v28, v28, v30
	v_add_f32_e32 v32, v32, v34
	v_add_f32_e32 v20, v20, v24
	v_add_f32_e32 v28, v28, v32
	v_add_f32_e32 v20, v20, v28
	v_add_f32_e32 v2, v2, v20
	v_max_f32_e32 v2, 0, v2
	v_mul_f32_e32 v3, 0x4f800000, v2
	v_cmp_gt_f32_e32 vcc, s8, v2
	s_nop 1
	v_cndmask_b32_e32 v2, v2, v3, vcc
	v_sqrt_f32_e32 v3, v2
	s_nop 0
	v_add_u32_e32 v4, -1, v3
	v_fma_f32 v5, -v4, v3, v2
	v_cmp_ge_f32_e64 s[18:19], 0, v5
	v_add_u32_e32 v5, 1, v3
	s_nop 0
	v_cndmask_b32_e64 v4, v3, v4, s[18:19]
	v_fma_f32 v3, -v5, v3, v2
	v_cmp_lt_f32_e64 s[18:19], 0, v3
	s_nop 1
	v_cndmask_b32_e64 v3, v4, v5, s[18:19]
	v_mul_f32_e32 v4, 0x37800000, v3
	v_cndmask_b32_e32 v3, v3, v4, vcc
	v_mov_b32_e32 v4, 0x260
	v_cmp_class_f32_e32 vcc, v2, v4
	s_nop 1
	v_cndmask_b32_e32 v2, v3, v2, vcc
	s_nop 1
	v_add_f32_dpp v3, v2, v2 quad_perm:[1,0,3,2] row_mask:0xf bank_mask:0xf
	s_nop 1
	v_add_f32_dpp v4, v3, v3 quad_perm:[2,3,0,1] row_mask:0xf bank_mask:0xf
	s_nop 1
	v_add_f32_dpp v5, v4, v4 row_half_mirror row_mask:0xf bank_mask:0xf
	s_nop 1
	v_add_f32_dpp v6, v5, v5 row_mirror row_mask:0xf bank_mask:0xf
	s_nop 1
	v_readlane_b32 s12, v6, 0
	v_readlane_b32 s13, v6, 16
	v_readlane_b32 s14, v6, 32
	v_readlane_b32 s15, v6, 48
	s_nop 3
	v_mov_b32_e32 v7, s12
	v_add_f32_e32 v7, s13, v7
	v_mov_b32_e32 v9, s14
	v_add_f32_e32 v9, s15, v9
	v_add_f32_e32 v0, v7, v9
	v_mov_b32_e32 v4, 0
	s_mov_b64 exec, 1
	v_cvt_f64_f32_e32 v[6:7], v0
	v_add_f64 v[8:9], v[6:7], s[4:5]
	global_atomic_add_f64 v[10:11], v4, v[8:9], s[6:7] sc0
	s_waitcnt vmcnt(0)
	v_cmp_le_f64_e32 vcc, s[16:17], v[10:11]
	s_and_saveexec_b64 s[2:3], vcc
	s_cbranch_execz .Lmain_end
	v_add_f64 v[10:11], v[10:11], -s[16:17]
	v_add_f64 v[10:11], v[10:11], v[6:7]
	v_cvt_f32_f64_e32 v0, v[10:11]
	v_mul_f32_e32 v0, 0x38000000, v0
	global_atomic_add_f32 v4, v0, s[10:11]
